# histogram reads issued before the row-load wait (on top of v55)
# speedup vs baseline: 1.0054x; 1.0019x over previous
.LBB0_720:
	s_or_b64 exec, exec, s[0:1]
	v_readfirstlane_b32 s8, v2
	s_cmp_gt_u32 s8, 31
	s_mov_b64 s[0:1], -1
	s_cbranch_scc1 .LBB0_715
	s_sub_i32 s0, 31, s8
	s_or_b32 s97, s0, s6
	s_lshl_b32 s1, s0, 14
	v_readlane_b32 s8, v254, 51
	s_add_u32 s8, s8, s1
	v_readlane_b32 s1, v254, 52
	v_mov_b32_e32 v10, v200
	s_addc_u32 s9, s1, 0
	s_mov_b32 s1, 0
	v_ashrrev_i32_e32 v11, 31, v10
	s_waitcnt lgkmcnt(0)
	v_lshl_add_u64 v[2:3], v[10:11], 2, s[8:9]
	s_mov_b64 s[10:11], 0x1000
	v_lshl_add_u64 v[4:5], v[2:3], 0, s[10:11]
	s_mov_b64 s[10:11], 0x2000
	v_lshl_add_u64 v[6:7], v[2:3], 0, s[10:11]
	s_mov_b64 s[10:11], 0x3000
	v_lshl_add_u64 v[8:9], v[2:3], 0, s[10:11]
	global_load_dword v77, v[2:3], off
	global_load_dword v76, v[2:3], off offset:256
	global_load_dword v75, v[2:3], off offset:512
	global_load_dword v74, v[2:3], off offset:768
	global_load_dword v73, v[2:3], off offset:1024
	global_load_dword v72, v[2:3], off offset:1280
	global_load_dword v71, v[2:3], off offset:1536
	global_load_dword v70, v[2:3], off offset:1792
	global_load_dword v69, v[2:3], off offset:2048
	global_load_dword v68, v[2:3], off offset:2304
	global_load_dword v67, v[2:3], off offset:2560
	global_load_dword v66, v[2:3], off offset:2816
	global_load_dword v65, v[2:3], off offset:3072
	global_load_dword v64, v[2:3], off offset:3328
	global_load_dword v63, v[2:3], off offset:3584
	global_load_dword v62, v[2:3], off offset:3840
	global_load_dword v61, v[4:5], off
	global_load_dword v60, v[4:5], off offset:256
	global_load_dword v59, v[4:5], off offset:512
	global_load_dword v58, v[4:5], off offset:768
	global_load_dword v57, v[4:5], off offset:1024
	global_load_dword v56, v[4:5], off offset:1280
	global_load_dword v55, v[4:5], off offset:1536
	global_load_dword v54, v[4:5], off offset:1792
	global_load_dword v53, v[4:5], off offset:2048
	global_load_dword v52, v[4:5], off offset:2304
	global_load_dword v51, v[4:5], off offset:2560
	global_load_dword v50, v[4:5], off offset:2816
	global_load_dword v49, v[4:5], off offset:3072
	global_load_dword v48, v[4:5], off offset:3328
	global_load_dword v47, v[4:5], off offset:3584
	global_load_dword v46, v[4:5], off offset:3840
	global_load_dword v45, v[6:7], off
	global_load_dword v44, v[6:7], off offset:256
	global_load_dword v43, v[6:7], off offset:512
	global_load_dword v42, v[6:7], off offset:768
	global_load_dword v41, v[6:7], off offset:1024
	global_load_dword v40, v[6:7], off offset:1280
	global_load_dword v39, v[6:7], off offset:1536
	global_load_dword v38, v[6:7], off offset:1792
	global_load_dword v37, v[6:7], off offset:2048
	global_load_dword v36, v[6:7], off offset:2304
	global_load_dword v35, v[6:7], off offset:2560
	global_load_dword v34, v[6:7], off offset:2816
	global_load_dword v33, v[6:7], off offset:3072
	global_load_dword v32, v[6:7], off offset:3328
	global_load_dword v31, v[6:7], off offset:3584
	global_load_dword v30, v[6:7], off offset:3840
	global_load_dword v29, v[8:9], off
	global_load_dword v28, v[8:9], off offset:256
	global_load_dword v27, v[8:9], off offset:512
	global_load_dword v26, v[8:9], off offset:768
	global_load_dword v25, v[8:9], off offset:1024
	global_load_dword v24, v[8:9], off offset:1280
	global_load_dword v23, v[8:9], off offset:1536
	global_load_dword v22, v[8:9], off offset:1792
	global_load_dword v21, v[8:9], off offset:2048
	global_load_dword v20, v[8:9], off offset:2304
	global_load_dword v19, v[8:9], off offset:2560
	global_load_dword v18, v[8:9], off offset:2816
	global_load_dword v17, v[8:9], off offset:3072
	global_load_dword v16, v[8:9], off offset:3328
	global_load_dword v15, v[8:9], off offset:3584
	global_load_dword v14, v[8:9], off offset:3840
	v_lshlrev_b32_e32 v11, 1, v10
	v_lshlrev_b64 v[2:3], v10, -1
	v_not_b32_e32 v12, v3
	v_not_b32_e32 v13, v2
	s_add_i32 s10, s6, 31
	s_lshr_b32 s10, s10, 10
	s_cmpk_lt_i32 s97, 0x100
	s_cbranch_scc1 .Lmk_nohist
	s_lshl_b32 s9, s0, 11
	v_lshl_add_u32 v6, v10, 5, s9
	ds_read_b128 v[2:5], v6
	ds_read_b128 v[6:9], v6 offset:16
.Lmk_nohist:
	s_waitcnt vmcnt(0)
	s_cmp_lt_u32 s10, 4
	s_cbranch_scc0 .Lmk_hi
	s_cmp_lt_u32 s10, 2
	s_cbranch_scc0 .Lmk_23
	s_cmp_eq_u32 s10, 0
	s_cbranch_scc1 .Lmk0
	s_branch .Lmk1

.Lmk_done:
	v_readlane_b32 s8, v255, 19
	s_cmpk_lt_i32 s97, 0x100
	s_cbranch_scc1 .LBB0_759
	s_lshl_b32 s0, s0, 11
	s_add_i32 s0, s0, 0
	s_mov_b32 s83, s78
	s_mov_b32 s77, s76
	s_mov_b32 s75, s74
	s_waitcnt lgkmcnt(1)
	v_add_u32_e32 v78, v2, v3
	v_add3_u32 v78, v78, v5, v4
	s_waitcnt lgkmcnt(0)
	v_add3_u32 v78, v78, v9, v8
	s_mov_b32 s73, s72
	s_mov_b32 s72, s70
	s_mov_b32 s76, s65
	s_mov_b32 s74, s63
	s_mov_b32 s69, s62
	s_mov_b32 s68, s58
	s_mov_b32 s66, s56
	s_mov_b32 s65, s55
	s_mov_b32 s64, s6
	s_mov_b32 s6, s51
	s_mov_b32 s58, s50
	s_mov_b64 s[62:63], s[48:49]
	s_mov_b32 s56, s43
	s_mov_b32 s49, s42
	s_mov_b32 s48, s41
	s_mov_b32 s91, s40
	s_mov_b32 s90, s39
	s_mov_b32 s89, s38
	s_mov_b32 s88, s2
	s_mov_b32 s2, s37
	s_mov_b32 s84, s7
	s_mov_b32 s7, s36
	s_mov_b32 s85, s35
	s_mov_b32 s44, s34
	s_mov_b32 s51, s31
	s_mov_b32 s50, s30
	s_mov_b32 s92, s29
	s_mov_b32 s71, s28
	s_mov_b32 s70, s27
	s_mov_b32 s81, s26
	s_mov_b32 s82, s25
	s_mov_b32 s55, s22
	v_add3_u32 v78, v78, v7, v6
	s_mov_b32 s9, 63
	s_nop 0
	v_readlane_b32 s25, v78, 63
	v_readlane_b32 s26, v78, 62
	v_readlane_b32 s27, v78, 61
	v_readlane_b32 s28, v78, 60
	v_readlane_b32 s29, v78, 59
	v_readlane_b32 s30, v78, 58
	v_readlane_b32 s31, v78, 57
	v_readlane_b32 s34, v78, 56
	v_readlane_b32 s35, v78, 55
	v_readlane_b32 s36, v78, 54
	v_readlane_b32 s37, v78, 53
	v_readlane_b32 s38, v78, 52
	v_readlane_b32 s39, v78, 51
	v_readlane_b32 s40, v78, 50
	v_readlane_b32 s41, v78, 49
	v_readlane_b32 s42, v78, 48
	s_mov_b32 s8, s1
	s_add_i32 s1, s8, s25
	s_cmpk_gt_u32 s1, 0xff
	s_cbranch_scc1 .Lthr_f63
	s_mov_b32 s8, s1
	s_add_i32 s1, s8, s26
	s_cmpk_gt_u32 s1, 0xff
	s_cbranch_scc1 .Lthr_f62
	s_mov_b32 s8, s1
	s_add_i32 s1, s8, s27
	s_cmpk_gt_u32 s1, 0xff
	s_cbranch_scc1 .Lthr_f61
	s_mov_b32 s8, s1
	s_add_i32 s1, s8, s28
	s_cmpk_gt_u32 s1, 0xff
	s_cbranch_scc1 .Lthr_f60
	s_mov_b32 s8, s1
	s_add_i32 s1, s8, s29
	s_cmpk_gt_u32 s1, 0xff
	s_cbranch_scc1 .Lthr_f59
	s_mov_b32 s8, s1
	s_add_i32 s1, s8, s30
	s_cmpk_gt_u32 s1, 0xff
	s_cbranch_scc1 .Lthr_f58
	s_mov_b32 s8, s1
	s_add_i32 s1, s8, s31
	s_cmpk_gt_u32 s1, 0xff
	s_cbranch_scc1 .Lthr_f57
	s_mov_b32 s8, s1
	s_add_i32 s1, s8, s34
	s_cmpk_gt_u32 s1, 0xff
	s_cbranch_scc1 .Lthr_f56
	s_mov_b32 s8, s1
	s_add_i32 s1, s8, s35
	s_cmpk_gt_u32 s1, 0xff
	s_cbranch_scc1 .Lthr_f55
	s_mov_b32 s8, s1
	s_add_i32 s1, s8, s36
	s_cmpk_gt_u32 s1, 0xff
	s_cbranch_scc1 .Lthr_f54
	s_mov_b32 s8, s1
	s_add_i32 s1, s8, s37
	s_cmpk_gt_u32 s1, 0xff
	s_cbranch_scc1 .Lthr_f53
	s_mov_b32 s8, s1
	s_add_i32 s1, s8, s38
	s_cmpk_gt_u32 s1, 0xff
	s_cbranch_scc1 .Lthr_f52
	s_mov_b32 s8, s1
	s_add_i32 s1, s8, s39
	s_cmpk_gt_u32 s1, 0xff
	s_cbranch_scc1 .Lthr_f51
	s_mov_b32 s8, s1
	s_add_i32 s1, s8, s40
	s_cmpk_gt_u32 s1, 0xff
	s_cbranch_scc1 .Lthr_f50
	s_mov_b32 s8, s1
	s_add_i32 s1, s8, s41
	s_cmpk_gt_u32 s1, 0xff
	s_cbranch_scc1 .Lthr_f49
	s_mov_b32 s8, s1
	s_add_i32 s1, s8, s42
	s_cmpk_gt_u32 s1, 0xff
	s_cbranch_scc1 .Lthr_f48
	s_mov_b32 s8, s1
	s_mov_b32 s9, 47
	s_branch .LBB0_723
